# baseline (speedup 1.0000x reference)
.LBB1_6:
	s_or_b64 exec, exec, s[4:5]
	s_lshr_b32 s5, s3, 8
	s_lshl_b32 s16, s20, 12
	s_lshl_b32 s4, s5, 5
	s_add_i32 s35, s16, 0
	s_add_u32 s18, s6, 0x18000
	v_and_b32_e32 v2, 12, v2
	v_bfe_u32 v0, v0, 2, 2
	s_addc_u32 s19, s7, 0
	v_bitop3_b32 v0, v2, v1, v0 bitop3:0x36
	s_add_u32 s16, s14, 0x8000
	v_lshlrev_b32_e32 v100, 4, v0
	v_or_b32_e32 v0, s4, v5
	s_addc_u32 s17, s15, 0
	s_lshl_b32 s36, s5, 7
	v_lshl_add_u32 v101, v0, 9, 0
	v_lshl_or_b32 v0, v1, 4, s36
	v_add_u32_e32 v0, 0, v0
	v_add_u32_e32 v83, v101, v100
	s_waitcnt vmcnt(0)
	s_waitcnt lgkmcnt(0)
	s_barrier
	s_lshl_b32 s40, s20, 14
	s_add_i32 s40, s40, 0x10000
	v_lshl_add_u32 v108, v5, 9, s40
	v_add_u32_e32 v109, v108, v100
	ds_read_b128 v[68:71], v109
	ds_read_b128 v[76:79], v109 offset:256
	v_xor_b32_e32 v109, 0x20, v100
	v_add_u32_e32 v109, v108, v109
	ds_read_b128 v[60:63], v109
	ds_read_b128 v[72:75], v109 offset:256
	v_xor_b32_e32 v109, 0x40, v100
	v_add_u32_e32 v109, v108, v109
	ds_read_b128 v[52:55], v109
	ds_read_b128 v[64:67], v109 offset:256
	v_xor_b32_e32 v109, 0x60, v100
	v_add_u32_e32 v109, v108, v109
	ds_read_b128 v[48:51], v109
	ds_read_b128 v[56:59], v109 offset:256
	v_xor_b32_e32 v109, 0x80, v100
	v_add_u32_e32 v109, v108, v109
	ds_read_b128 v[36:39], v109
	ds_read_b128 v[44:47], v109 offset:256
	v_xor_b32_e32 v109, 0xa0, v100
	v_add_u32_e32 v109, v108, v109
	ds_read_b128 v[28:31], v109
	ds_read_b128 v[40:43], v109 offset:256
	v_xor_b32_e32 v109, 0xc0, v100
	v_add_u32_e32 v109, v108, v109
	ds_read_b128 v[24:27], v109
	ds_read_b128 v[32:35], v109 offset:256
	v_xor_b32_e32 v109, 0xe0, v100
	v_add_u32_e32 v109, v108, v109
	ds_read_b128 v[20:23], v109
	ds_read_b128 v[16:19], v109 offset:256
	s_waitcnt lgkmcnt(0)
	s_barrier
	s_add_u32 s40, s6, 0x10000
	s_addc_u32 s41, s7, 0
	s_mov_b32 s42, m0
	s_mov_b32 m0, s27
	s_nop 0
	global_load_lds_dwordx4 v192, s[40:41]
	s_mov_b32 m0, s42
	s_add_u32 s40, s6, 0x12000
	s_addc_u32 s41, s7, 0
	s_mov_b32 s42, m0
	s_mov_b32 m0, s28
	s_nop 0
	global_load_lds_dwordx4 v192, s[40:41]
	s_mov_b32 m0, s42
	s_add_u32 s40, s6, 0x14000
	s_addc_u32 s41, s7, 0
	s_mov_b32 s42, m0
	s_mov_b32 m0, s29
	s_nop 0
	global_load_lds_dwordx4 v192, s[40:41]
	s_mov_b32 m0, s42
	s_add_u32 s40, s6, 0x16000
	s_addc_u32 s41, s7, 0
	s_mov_b32 s42, m0
	s_mov_b32 m0, s30
	s_nop 0
	global_load_lds_dwordx4 v192, s[40:41]
	s_mov_b32 m0, s42
	v_add_u32_e32 v80, 0x22000, v0
	ds_read_b128 v[84:87], v83
	ds_read_b128 v[0:3], v80
	ds_read_b128 v[4:7], v80 offset:32
	ds_read_b128 v[8:11], v80 offset:64
	ds_read_b128 v[12:15], v80 offset:96
	ds_read_b128 v[88:91], v83 offset:256
	s_waitcnt vmcnt(15) lgkmcnt(1)
	v_mfma_f32_32x32x16_bf16 v[0:15], v[84:87], v[68:71], v[0:15]
	v_xor_b32_e32 v102, 32, v100
	v_add_u32_e32 v84, v101, v102
	v_xor_b32_e32 v103, 64, v100
	v_add_u32_e32 v85, v101, v103
	v_xor_b32_e32 v104, 0x60, v100
	v_xor_b32_e32 v105, 0x80, v100
	v_xor_b32_e32 v106, 0xa0, v100
	s_waitcnt vmcnt(7) lgkmcnt(0)
	v_mfma_f32_32x32x16_bf16 v[0:15], v[88:91], v[76:79], v[0:15]
	ds_read_b128 v[86:89], v84
	ds_read_b128 v[90:93], v84 offset:256
	v_xor_b32_e32 v107, 0xe0, v100
	v_lshl_add_u32 v81, v81, 4, s35
	v_add_u32_e32 v81, 0x18000, v81
	v_lshl_add_u32 v82, s5, 11, v81
	s_add_u32 s36, s6, 0x1a000
	s_addc_u32 s37, s7, 0
	s_waitcnt lgkmcnt(1)
	v_mfma_f32_32x32x16_bf16 v[0:15], v[86:89], v[60:63], v[0:15]
	s_add_u32 s38, s6, 0x1c000
	s_addc_u32 s39, s7, 0
	s_add_u32 s6, s6, 0x1e000
	s_addc_u32 s7, s7, 0
	s_waitcnt vmcnt(6) lgkmcnt(0)
	v_mfma_f32_32x32x16_bf16 v[0:15], v[90:93], v[72:75], v[0:15]
	ds_read_b128 v[86:89], v85
	ds_read_b128 v[90:93], v85 offset:256
	s_waitcnt lgkmcnt(1)
	v_mfma_f32_32x32x16_bf16 v[0:15], v[86:89], v[52:55], v[0:15]
	v_add_u32_e32 v86, v101, v104
	v_add_u32_e32 v87, v101, v105
	s_waitcnt vmcnt(5) lgkmcnt(0)
	v_mfma_f32_32x32x16_bf16 v[0:15], v[90:93], v[64:67], v[0:15]
	ds_read_b128 v[88:91], v86
	ds_read_b128 v[92:95], v86 offset:256
	s_waitcnt lgkmcnt(1)
	v_mfma_f32_32x32x16_bf16 v[0:15], v[88:91], v[48:51], v[0:15]
	s_waitcnt vmcnt(4) lgkmcnt(0)
	v_mfma_f32_32x32x16_bf16 v[0:15], v[92:95], v[56:59], v[0:15]
	ds_read_b128 v[88:91], v87
	ds_read_b128 v[92:95], v87 offset:256
	s_waitcnt lgkmcnt(1)
	v_mfma_f32_32x32x16_bf16 v[0:15], v[88:91], v[36:39], v[0:15]
	v_add_u32_e32 v88, v101, v106
	v_add_u32_e32 v89, v101, v107
	s_waitcnt vmcnt(3) lgkmcnt(0)
	v_mfma_f32_32x32x16_bf16 v[0:15], v[92:95], v[44:47], v[0:15]
	ds_read_b128 v[90:93], v88
	ds_read_b128 v[94:97], v88 offset:256
	s_waitcnt lgkmcnt(1)
	v_mfma_f32_32x32x16_bf16 v[0:15], v[90:93], v[28:31], v[0:15]
	v_xor_b32_e32 v91, 0xc0, v100
	v_add_u32_e32 v90, v101, v91
	v_add_u32_e32 v101, 0x10000, v101
	v_add_u32_e32 v100, v101, v100
	v_add_u32_e32 v91, v101, v91
	s_waitcnt vmcnt(2) lgkmcnt(0)
	v_mfma_f32_32x32x16_bf16 v[0:15], v[94:97], v[40:43], v[0:15]
	ds_read_b128 v[92:95], v90
	ds_read_b128 v[96:99], v90 offset:256
	s_waitcnt lgkmcnt(1)
	v_mfma_f32_32x32x16_bf16 v[0:15], v[92:95], v[24:27], v[0:15]
	ds_read_b128 v[92:95], v89
	s_waitcnt vmcnt(1) lgkmcnt(1)
	v_mfma_f32_32x32x16_bf16 v[0:15], v[96:99], v[32:35], v[0:15]
	ds_read_b128 v[96:99], v89 offset:256
	s_waitcnt lgkmcnt(1)
	v_mfma_f32_32x32x16_bf16 v[0:15], v[92:95], v[20:23], v[0:15]
	s_waitcnt vmcnt(0) lgkmcnt(0)
	v_mfma_f32_32x32x16_bf16 v[0:15], v[96:99], v[16:19], v[0:15]
	s_nop 11
	v_cvt_pk_bf16_f32 v0, v0, v1
	v_cvt_pk_bf16_f32 v1, v2, v3
	v_cvt_pk_bf16_f32 v2, v4, v5
	v_cvt_pk_bf16_f32 v3, v6, v7
	v_cvt_pk_bf16_f32 v4, v8, v9
	v_cvt_pk_bf16_f32 v5, v10, v11
	v_cvt_pk_bf16_f32 v6, v12, v13
	v_cvt_pk_bf16_f32 v7, v14, v15
	ds_write_b128 v82, v[0:3]
	ds_write_b128 v82, v[4:7] offset:1024
	ds_read_b128 v[0:3], v80 offset:256
	ds_read2_b32 v[4:5], v80 offset0:72 offset1:73
	ds_read2_b32 v[6:7], v80 offset0:74 offset1:75
	ds_read2_b32 v[8:9], v80 offset0:80 offset1:81
	ds_read2_b32 v[10:11], v80 offset0:82 offset1:83
	ds_read2_b32 v[12:13], v80 offset0:88 offset1:89
	ds_read2_b32 v[14:15], v80 offset0:90 offset1:91
	ds_read_b128 v[92:95], v83 offset:32768
	ds_read_b128 v[96:99], v83 offset:33024
	s_waitcnt lgkmcnt(0)
	s_barrier
	v_mfma_f32_32x32x16_bf16 v[0:15], v[92:95], v[68:71], v[0:15]
	s_mov_b32 s5, m0
	s_mov_b32 m0, s21
	s_nop 0
	global_load_lds_dwordx4 v192, s[18:19]
	s_mov_b32 m0, s5
	v_mfma_f32_32x32x16_bf16 v[0:15], v[96:99], v[76:79], v[0:15]
	ds_read_b128 v[92:95], v84 offset:32768
	ds_read_b128 v[96:99], v84 offset:33024
	s_mov_b32 s5, m0
	s_mov_b32 m0, s31
	s_nop 0
	global_load_lds_dwordx4 v192, s[36:37]
	s_mov_b32 m0, s5
	s_waitcnt lgkmcnt(1)
	v_mfma_f32_32x32x16_bf16 v[0:15], v[92:95], v[60:63], v[0:15]
	s_mov_b32 s5, m0
	s_mov_b32 m0, s33
	s_nop 0
	global_load_lds_dwordx4 v192, s[38:39]
	s_mov_b32 m0, s5
	s_waitcnt lgkmcnt(0)
	v_mfma_f32_32x32x16_bf16 v[0:15], v[96:99], v[72:75], v[0:15]
	s_mov_b32 s5, m0
	s_mov_b32 m0, s34
	s_nop 0
	global_load_lds_dwordx4 v192, s[6:7]
	s_mov_b32 m0, s5
	s_add_u32 s6, s14, 0x2000
	s_addc_u32 s7, s15, 0
	s_add_u32 s18, s14, 0x4000
	s_addc_u32 s19, s15, 0
	s_add_u32 s34, s14, 0x6000
	s_addc_u32 s35, s15, 0
	ds_read_b128 v[92:95], v85 offset:32768
	ds_read_b128 v[96:99], v85 offset:33024
	s_waitcnt lgkmcnt(1)
	v_mfma_f32_32x32x16_bf16 v[0:15], v[92:95], v[52:55], v[0:15]
	s_waitcnt lgkmcnt(0)
	v_mfma_f32_32x32x16_bf16 v[0:15], v[96:99], v[64:67], v[0:15]
	ds_read_b128 v[92:95], v86 offset:32768
	ds_read_b128 v[96:99], v86 offset:33024
	s_waitcnt lgkmcnt(1)
	v_mfma_f32_32x32x16_bf16 v[0:15], v[92:95], v[48:51], v[0:15]
	s_waitcnt lgkmcnt(0)
	v_mfma_f32_32x32x16_bf16 v[0:15], v[96:99], v[56:59], v[0:15]
	ds_read_b128 v[92:95], v87 offset:32768
	ds_read_b128 v[96:99], v87 offset:33024
	s_waitcnt lgkmcnt(1)
	v_mfma_f32_32x32x16_bf16 v[0:15], v[92:95], v[36:39], v[0:15]
	s_waitcnt lgkmcnt(0)
	v_mfma_f32_32x32x16_bf16 v[0:15], v[96:99], v[44:47], v[0:15]
	ds_read_b128 v[92:95], v88 offset:32768
	ds_read_b128 v[96:99], v88 offset:33024
	s_waitcnt lgkmcnt(1)
	v_mfma_f32_32x32x16_bf16 v[0:15], v[92:95], v[28:31], v[0:15]
	s_waitcnt lgkmcnt(0)
	v_mfma_f32_32x32x16_bf16 v[0:15], v[96:99], v[40:43], v[0:15]
	ds_read_b128 v[92:95], v90 offset:32768
	ds_read_b128 v[96:99], v90 offset:33024
	s_waitcnt lgkmcnt(1)
	v_mfma_f32_32x32x16_bf16 v[0:15], v[92:95], v[24:27], v[0:15]
	ds_read_b128 v[92:95], v89 offset:32768
	s_waitcnt lgkmcnt(1)
	v_mfma_f32_32x32x16_bf16 v[0:15], v[96:99], v[32:35], v[0:15]
	ds_read_b128 v[96:99], v89 offset:33024
	ds_read_b128 v[128:131], v81
	ds_read_b128 v[132:135], v81 offset:1024
	ds_read_b128 v[136:139], v81 offset:2048
	ds_read_b128 v[140:143], v81 offset:3072
	s_waitcnt lgkmcnt(5)
	v_mfma_f32_32x32x16_bf16 v[0:15], v[92:95], v[20:23], v[0:15]
	s_waitcnt lgkmcnt(4)
	v_mfma_f32_32x32x16_bf16 v[0:15], v[96:99], v[16:19], v[0:15]
	s_nop 11
	v_cvt_pk_bf16_f32 v0, v0, v1
	v_cvt_pk_bf16_f32 v1, v2, v3
	v_cvt_pk_bf16_f32 v2, v4, v5
	v_cvt_pk_bf16_f32 v3, v6, v7
	v_cvt_pk_bf16_f32 v4, v8, v9
	v_cvt_pk_bf16_f32 v5, v10, v11
	v_cvt_pk_bf16_f32 v6, v12, v13
	v_cvt_pk_bf16_f32 v7, v14, v15
	ds_write_b128 v82, v[0:3] offset:20480
	ds_write_b128 v82, v[4:7] offset:21504
	ds_read_b128 v[0:3], v80 offset:512
	ds_read2_b32 v[4:5], v80 offset0:136 offset1:137
	ds_read2_b32 v[6:7], v80 offset0:138 offset1:139
	ds_read2_b32 v[8:9], v80 offset0:144 offset1:145
	ds_read2_b32 v[10:11], v80 offset0:146 offset1:147
	ds_read2_b32 v[12:13], v80 offset0:152 offset1:153
	ds_read2_b32 v[14:15], v80 offset0:154 offset1:155
	s_waitcnt vmcnt(4) lgkmcnt(0)
	s_barrier
	ds_read_b128 v[92:95], v100
	ds_read_b128 v[96:99], v100 offset:256
	s_mov_b32 s5, m0
	s_mov_b32 m0, s23
	s_nop 0
	global_load_lds_dwordx4 v192, s[14:15]
	s_mov_b32 m0, s5
	s_waitcnt lgkmcnt(1)
	v_mfma_f32_32x32x16_bf16 v[0:15], v[92:95], v[68:71], v[0:15]
	v_add_u32_e32 v100, v101, v102
	s_mov_b32 s5, m0
	s_mov_b32 m0, s24
	s_nop 0
	global_load_lds_dwordx4 v192, s[6:7]
	s_mov_b32 m0, s5
	s_add_u32 s6, s14, 0xa000
	s_waitcnt lgkmcnt(0)
	v_mfma_f32_32x32x16_bf16 v[0:15], v[96:99], v[76:79], v[0:15]
	ds_read_b128 v[92:95], v100
	ds_read_b128 v[96:99], v100 offset:256
	v_add_u32_e32 v100, v101, v103
	s_mov_b32 s5, m0
	s_mov_b32 m0, s25
	s_nop 0
	global_load_lds_dwordx4 v192, s[18:19]
	s_mov_b32 m0, s5
	s_addc_u32 s7, s15, 0
	s_waitcnt lgkmcnt(1)
	v_mfma_f32_32x32x16_bf16 v[0:15], v[92:95], v[60:63], v[0:15]
	s_mov_b32 s5, m0
	s_mov_b32 m0, s26
	s_nop 0
	global_load_lds_dwordx4 v192, s[34:35]
	s_mov_b32 m0, s5
	s_add_u32 s18, s14, 0xc000
	s_addc_u32 s19, s15, 0
	s_add_u32 s34, s14, 0xe000
	s_addc_u32 s35, s15, 0
	s_cmpk_gt_u32 s3, 0xff
	s_waitcnt lgkmcnt(0)
	v_mfma_f32_32x32x16_bf16 v[0:15], v[96:99], v[72:75], v[0:15]
	ds_read_b128 v[92:95], v100
	ds_read_b128 v[96:99], v100 offset:256
	v_add_u32_e32 v100, v101, v104
	s_waitcnt lgkmcnt(1)
	v_mfma_f32_32x32x16_bf16 v[0:15], v[92:95], v[52:55], v[0:15]
	s_waitcnt lgkmcnt(0)
	v_mfma_f32_32x32x16_bf16 v[0:15], v[96:99], v[64:67], v[0:15]
	ds_read_b128 v[92:95], v100
	ds_read_b128 v[96:99], v100 offset:256
	v_add_u32_e32 v100, v101, v105
	s_waitcnt lgkmcnt(1)
	v_mfma_f32_32x32x16_bf16 v[0:15], v[92:95], v[48:51], v[0:15]
	s_waitcnt lgkmcnt(0)
	v_mfma_f32_32x32x16_bf16 v[0:15], v[96:99], v[56:59], v[0:15]
	ds_read_b128 v[92:95], v100
	ds_read_b128 v[96:99], v100 offset:256
	v_add_u32_e32 v100, v101, v106
	s_waitcnt lgkmcnt(1)
	v_mfma_f32_32x32x16_bf16 v[0:15], v[92:95], v[36:39], v[0:15]
	s_waitcnt lgkmcnt(0)
	v_mfma_f32_32x32x16_bf16 v[0:15], v[96:99], v[44:47], v[0:15]
	ds_read_b128 v[92:95], v100
	ds_read_b128 v[96:99], v100 offset:256
	s_waitcnt lgkmcnt(1)
	v_mfma_f32_32x32x16_bf16 v[0:15], v[92:95], v[28:31], v[0:15]
	s_waitcnt lgkmcnt(0)
	v_mfma_f32_32x32x16_bf16 v[0:15], v[96:99], v[40:43], v[0:15]
	ds_read_b128 v[92:95], v91
	ds_read_b128 v[96:99], v91 offset:256
	v_add_u32_e32 v91, v101, v107
	s_waitcnt lgkmcnt(1)
	v_mfma_f32_32x32x16_bf16 v[0:15], v[92:95], v[24:27], v[0:15]
	ds_read_b128 v[92:95], v91
	s_waitcnt lgkmcnt(1)
	v_mfma_f32_32x32x16_bf16 v[0:15], v[96:99], v[32:35], v[0:15]
	ds_read_b128 v[96:99], v91 offset:256
	ds_read_b128 v[144:147], v81 offset:20480
	ds_read_b128 v[148:151], v81 offset:21504
	ds_read_b128 v[152:155], v81 offset:22528
	ds_read_b128 v[156:159], v81 offset:23552
	s_waitcnt lgkmcnt(5)
	v_mfma_f32_32x32x16_bf16 v[0:15], v[92:95], v[20:23], v[0:15]
	s_waitcnt lgkmcnt(4)
	v_mfma_f32_32x32x16_bf16 v[0:15], v[96:99], v[16:19], v[0:15]
	s_nop 11
	v_cvt_pk_bf16_f32 v0, v0, v1
	v_cvt_pk_bf16_f32 v1, v2, v3
	v_cvt_pk_bf16_f32 v2, v4, v5
	v_cvt_pk_bf16_f32 v3, v6, v7
	v_cvt_pk_bf16_f32 v4, v8, v9
	v_cvt_pk_bf16_f32 v5, v10, v11
	v_cvt_pk_bf16_f32 v6, v12, v13
	v_cvt_pk_bf16_f32 v7, v14, v15
	ds_write_b128 v82, v[0:3]
	ds_write_b128 v82, v[4:7] offset:1024
	ds_read_b128 v[0:3], v80 offset:768
	ds_read2_b32 v[4:5], v80 offset0:200 offset1:201
	ds_read2_b32 v[6:7], v80 offset0:202 offset1:203
	ds_read2_b32 v[8:9], v80 offset0:208 offset1:209
	ds_read2_b32 v[10:11], v80 offset0:210 offset1:211
	ds_read2_b32 v[12:13], v80 offset0:216 offset1:217
	ds_read2_b32 v[14:15], v80 offset0:218 offset1:219
	s_waitcnt vmcnt(4) lgkmcnt(0)
	s_barrier
	ds_read_b128 v[92:95], v83
	ds_read_b128 v[96:99], v83 offset:256
	s_mov_b32 s5, m0
	s_mov_b32 m0, s27
	s_nop 0
	global_load_lds_dwordx4 v192, s[16:17]
	s_mov_b32 m0, s5
	s_waitcnt lgkmcnt(1)
	v_mfma_f32_32x32x16_bf16 v[0:15], v[92:95], v[68:71], v[0:15]
	s_mov_b32 s5, m0
	s_mov_b32 m0, s28
	s_nop 0
	global_load_lds_dwordx4 v192, s[6:7]
	s_mov_b32 m0, s5
	s_movk_i32 s7, 0x80
	s_waitcnt lgkmcnt(0)
	v_mfma_f32_32x32x16_bf16 v[0:15], v[96:99], v[76:79], v[0:15]
	ds_read_b128 v[68:71], v84
	ds_read_b128 v[76:79], v84 offset:256
	s_mov_b32 s5, m0
	s_mov_b32 m0, s29
	s_nop 0
	global_load_lds_dwordx4 v192, s[18:19]
	s_mov_b32 m0, s5
	s_movk_i32 s6, 0xc0
	s_waitcnt lgkmcnt(1)
	v_mfma_f32_32x32x16_bf16 v[0:15], v[68:71], v[60:63], v[0:15]
	s_mov_b32 s5, m0
	s_mov_b32 m0, s30
	s_nop 0
	global_load_lds_dwordx4 v192, s[34:35]
	s_mov_b32 m0, s5
	s_mov_b32 s5, 0x10000
	ds_read_b128 v[60:63], v85
	ds_read_b128 v[68:71], v85 offset:256
	s_waitcnt lgkmcnt(2)
	v_mfma_f32_32x32x16_bf16 v[0:15], v[76:79], v[72:75], v[0:15]
	s_waitcnt lgkmcnt(1)
	v_mfma_f32_32x32x16_bf16 v[0:15], v[60:63], v[52:55], v[0:15]
	ds_read_b128 v[52:55], v86
	ds_read_b128 v[60:63], v86 offset:256
	s_waitcnt lgkmcnt(2)
	v_mfma_f32_32x32x16_bf16 v[0:15], v[68:71], v[64:67], v[0:15]
	s_waitcnt lgkmcnt(1)
	v_mfma_f32_32x32x16_bf16 v[0:15], v[52:55], v[48:51], v[0:15]
	ds_read_b128 v[48:51], v87
	ds_read_b128 v[52:55], v87 offset:256
	s_waitcnt lgkmcnt(2)
	v_mfma_f32_32x32x16_bf16 v[0:15], v[60:63], v[56:59], v[0:15]
	s_waitcnt lgkmcnt(1)
	v_mfma_f32_32x32x16_bf16 v[0:15], v[48:51], v[36:39], v[0:15]
	s_waitcnt lgkmcnt(0)
	v_mfma_f32_32x32x16_bf16 v[0:15], v[52:55], v[44:47], v[0:15]
	ds_read_b128 v[36:39], v88
	ds_read_b128 v[44:47], v88 offset:256
	s_waitcnt lgkmcnt(1)
	v_mfma_f32_32x32x16_bf16 v[0:15], v[36:39], v[28:31], v[0:15]
	ds_read_b128 v[28:31], v90
	ds_read_b128 v[36:39], v90 offset:256
	s_waitcnt lgkmcnt(2)
	v_mfma_f32_32x32x16_bf16 v[0:15], v[44:47], v[40:43], v[0:15]
	s_waitcnt lgkmcnt(1)
	v_mfma_f32_32x32x16_bf16 v[0:15], v[28:31], v[24:27], v[0:15]
	ds_read_b128 v[24:27], v89
	ds_read_b128 v[28:31], v89 offset:256
	ds_read_b128 v[160:163], v81
	ds_read_b128 v[164:167], v81 offset:1024
	ds_read_b128 v[168:171], v81 offset:2048
	ds_read_b128 v[172:175], v81 offset:3072
	s_waitcnt lgkmcnt(6)
	v_mfma_f32_32x32x16_bf16 v[0:15], v[36:39], v[32:35], v[0:15]
	s_waitcnt lgkmcnt(5)
	v_mfma_f32_32x32x16_bf16 v[0:15], v[24:27], v[20:23], v[0:15]
	v_mbcnt_lo_u32_b32 v20, -1, 0
	v_mbcnt_hi_u32_b32 v193, -1, v20
	v_mov_b32_e32 v194, v193
	s_waitcnt lgkmcnt(4)
	v_mfma_f32_32x32x16_bf16 v[0:15], v[28:31], v[16:19], v[0:15]
	s_nop 11
	v_cvt_pk_bf16_f32 v0, v0, v1
	v_cvt_pk_bf16_f32 v1, v2, v3
	v_cvt_pk_bf16_f32 v2, v4, v5
	v_cvt_pk_bf16_f32 v3, v6, v7
	v_cvt_pk_bf16_f32 v4, v8, v9
	v_cvt_pk_bf16_f32 v5, v10, v11
	v_cvt_pk_bf16_f32 v6, v12, v13
	v_cvt_pk_bf16_f32 v7, v14, v15
	ds_write_b128 v82, v[0:3] offset:20480
	ds_write_b128 v82, v[4:7] offset:21504
	s_waitcnt vmcnt(4) lgkmcnt(0)
	s_barrier
	ds_read_b128 v[176:179], v81 offset:20480
	ds_read_b128 v[180:183], v81 offset:21504
	ds_read_b128 v[184:187], v81 offset:22528
	ds_read_b128 v[188:191], v81 offset:23552
	s_waitcnt lgkmcnt(0)
	s_barrier
	s_nop 0
	v_and_b32_e32 v196, 31, v194
	v_ashrrev_i32_e32 v197, 5, v194
	v_lshlrev_b32_e32 v195, 2, v194
	v_bfe_u32 v198, v194, 2, 2
	s_cbranch_scc0 .LBB1_16
	v_lshl_add_u32 v0, s20, 2, v197
	v_lshlrev_b32_e32 v3, 2, v197
	v_add_u32_e32 v1, 2, v0
	v_lshlrev_b32_e32 v2, 9, v0
	v_and_b32_e32 v3, 12, v3
	v_bfe_u32 v0, v0, 2, 2
	v_bitop3_b32 v0, v0, v196, v3 bitop3:0x36
	v_lshl_or_b32 v199, v0, 4, v2
	v_lshlrev_b32_e32 v0, 2, v1
	s_bfe_u32 s18, s3, 0x10006
	v_and_b32_e32 v0, 12, v0
	v_bfe_u32 v2, v1, 2, 2
	v_bitop3_b32 v0, v0, v196, v2 bitop3:0x36
	v_lshrrev_b32_e32 v2, 3, v194
	s_lshl_b32 s16, s18, 8
	v_and_b32_e32 v2, 2, v2
	v_bfe_u32 v3, v194, 1, 1
	s_add_i32 s16, s16, 0
	v_lshlrev_b32_e32 v4, 3, v194
	v_lshl_add_u32 v5, v197, 11, s16
	v_bitop3_b32 v2, v2, v197, v3 bitop3:0x36
	v_and_or_b32 v4, v4, 8, v5
	v_lshlrev_b32_e32 v2, 4, v2
	v_lshlrev_b32_e32 v3, 6, v198
	v_lshl_add_u32 v4, v198, 9, v4
	v_or_b32_e32 v5, v2, v3
	v_add_u32_e32 v200, v4, v5
	v_bitop3_b32 v5, v2, v3, 32 bitop3:0xde
	v_add_u32_e32 v6, 0x1000, v4
	v_add_u32_e32 v201, v6, v5
	v_xor_b32_e32 v5, 64, v3
	v_bitop3_b32 v5, v2, v5, 32 bitop3:0xde
	v_add_u32_e32 v203, v6, v5
	v_xor_b32_e32 v5, 0x80, v3
	v_bitop3_b32 v7, v2, v3, 64 bitop3:0xf6
	v_bitop3_b32 v5, v2, v5, 32 bitop3:0xde
	v_add_u32_e32 v202, v4, v7
	v_bitop3_b32 v7, v2, v3, s7 bitop3:0xf6
	v_add_u32_e32 v205, v6, v5
	v_xor_b32_e32 v5, 0xc0, v3
	v_bitop3_b32 v3, v2, v3, s6 bitop3:0xf6
	s_and_b32 s6, s22, 2
	v_lshlrev_b32_e32 v1, 9, v1
	s_lshl_b32 s27, s6, 2
	s_lshl_b32 s7, s6, 8
	s_lshl_b32 s6, s6, 12
	v_lshl_or_b32 v208, v0, 4, v1
	s_lshl_b32 s19, s20, 11
	s_add_i32 s7, s7, 0
	s_add_i32 s6, s6, 0
	v_mov_b32_e32 v0, 0
	v_bitop3_b32 v2, v2, v5, 32 bitop3:0xde
	s_waitcnt vmcnt(0)
	s_add_i32 s19, s19, 0
	s_add_i32 s16, s7, 0x20000
	s_add_i32 s7, s7, 0x20100
	v_lshlrev_b32_e32 v209, 4, v194
	s_add_i32 s6, s6, 0x18000
	v_mov_b32_e32 v14, v0
	v_mov_b32_e32 v15, v0
	v_add_u32_e32 v204, v4, v7
	v_add_u32_e32 v206, v4, v3
	v_add_u32_e32 v207, v6, v2
	v_add_u32_e32 v212, s6, v209
	s_add_u32 s6, s8, 0xfff90000
	v_mov_b32_e32 v1, v0
	v_mov_b32_e32 v2, v0
	v_mov_b32_e32 v3, v0
	v_mov_b32_e32 v4, v0
	v_mov_b32_e32 v5, v0
	v_mov_b32_e32 v6, v0
	v_mov_b32_e32 v7, v0
	v_mov_b32_e32 v8, v0
	v_mov_b32_e32 v9, v0
	v_mov_b32_e32 v10, v0
	v_mov_b32_e32 v11, v0
	v_mov_b32_e32 v12, v0
	v_mov_b32_e32 v13, v0
	v_mov_b64_e32 v[62:63], v[14:15]
	v_mov_b64_e32 v[94:95], v[14:15]
	v_mov_b64_e32 v[126:127], v[14:15]
	v_mov_b64_e32 v[30:31], v[14:15]
	v_mov_b64_e32 v[46:47], v[14:15]
	v_mov_b64_e32 v[78:79], v[14:15]
	v_mov_b64_e32 v[110:111], v[14:15]
	v_add_u32_e32 v210, s16, v195
	v_add_u32_e32 v211, s7, v195
	s_addc_u32 s7, s9, -1
	s_mov_b32 s33, 1
	s_mov_b32 s31, 0x8000
	s_mov_b32 s29, 0x10000
	v_mov_b64_e32 v[60:61], v[12:13]
	v_mov_b64_e32 v[58:59], v[10:11]
	v_mov_b64_e32 v[56:57], v[8:9]
	v_mov_b64_e32 v[54:55], v[6:7]
	v_mov_b64_e32 v[52:53], v[4:5]
	v_mov_b64_e32 v[50:51], v[2:3]
	v_mov_b64_e32 v[48:49], v[0:1]
	v_mov_b64_e32 v[92:93], v[12:13]
	v_mov_b64_e32 v[90:91], v[10:11]
	v_mov_b64_e32 v[88:89], v[8:9]
	v_mov_b64_e32 v[86:87], v[6:7]
	v_mov_b64_e32 v[84:85], v[4:5]
	v_mov_b64_e32 v[82:83], v[2:3]
	v_mov_b64_e32 v[80:81], v[0:1]
	v_mov_b64_e32 v[124:125], v[12:13]
	v_mov_b64_e32 v[122:123], v[10:11]
	v_mov_b64_e32 v[120:121], v[8:9]
	v_mov_b64_e32 v[118:119], v[6:7]
	v_mov_b64_e32 v[116:117], v[4:5]
	v_mov_b64_e32 v[114:115], v[2:3]
	v_mov_b64_e32 v[112:113], v[0:1]
	v_mov_b64_e32 v[28:29], v[12:13]
	v_mov_b64_e32 v[26:27], v[10:11]
	v_mov_b64_e32 v[24:25], v[8:9]
	v_mov_b64_e32 v[22:23], v[6:7]
	v_mov_b64_e32 v[20:21], v[4:5]
	v_mov_b64_e32 v[18:19], v[2:3]
	v_mov_b64_e32 v[16:17], v[0:1]
	v_mov_b64_e32 v[44:45], v[12:13]
	v_mov_b64_e32 v[42:43], v[10:11]
	v_mov_b64_e32 v[40:41], v[8:9]
	v_mov_b64_e32 v[38:39], v[6:7]
	v_mov_b64_e32 v[36:37], v[4:5]
	v_mov_b64_e32 v[34:35], v[2:3]
	v_mov_b64_e32 v[32:33], v[0:1]
	v_mov_b64_e32 v[76:77], v[12:13]
	v_mov_b64_e32 v[74:75], v[10:11]
	v_mov_b64_e32 v[72:73], v[8:9]
	v_mov_b64_e32 v[70:71], v[6:7]
	v_mov_b64_e32 v[68:69], v[4:5]
	v_mov_b64_e32 v[66:67], v[2:3]
	v_mov_b64_e32 v[64:65], v[0:1]
	v_mov_b64_e32 v[108:109], v[12:13]
	v_mov_b64_e32 v[106:107], v[10:11]
	v_mov_b64_e32 v[104:105], v[8:9]
	v_mov_b64_e32 v[102:103], v[6:7]
	v_mov_b64_e32 v[100:101], v[4:5]
	v_mov_b64_e32 v[98:99], v[2:3]
	v_mov_b64_e32 v[96:97], v[0:1]
	s_waitcnt lgkmcnt(0)
	s_barrier
